# P9 final sum+LN2 hand-written: double-buffered rows, next row's loads in flight during reduce/normalise/store
# speedup vs baseline: 1.0063x; 1.0063x over previous
.LBB0_1221:
	s_and_b64 vcc, exec, s[0:1]
	s_cbranch_vccnz .LBB0_1225
	s_lshl_b32 s0, s94, 3
	v_readlane_b32 s1, v252, 6
	s_add_i32 s2, s1, s0
	s_cmpk_gt_i32 s2, 0x1fff
	s_cbranch_scc1 .LBB0_1225
	v_lshlrev_b32_e32 v224, 2, v214
	v_lshlrev_b32_e32 v225, 3, v214
	v_lshlrev_b32_e32 v226, 4, v214
	v_add_u32_e32 v227, 0x1000, v226
	v_xor_b32_e32 v228, 1, v214
	v_xor_b32_e32 v229, 2, v214
	v_xor_b32_e32 v230, 4, v214
	v_xor_b32_e32 v231, 8, v214
	v_xor_b32_e32 v232, 16, v214
	v_xor_b32_e32 v233, 32, v214
	v_lshlrev_b32_e32 v228, 2, v228
	v_lshlrev_b32_e32 v229, 2, v229
	v_lshlrev_b32_e32 v230, 2, v230
	v_lshlrev_b32_e32 v231, 2, v231
	v_lshlrev_b32_e32 v232, 2, v232
	v_lshlrev_b32_e32 v233, 2, v233
	s_lshl_b32 s9, s90, 3
	s_mov_b32 s8, 0x3f9837f0
	s_mov_b32 s23, 0xf800000
	s_movk_i32 s22, 0x260
	s_add_u32 s4, s96, 0x12800000
	s_addc_u32 s5, s97, 0
	s_add_u32 s6, s96, 0xe800000
	s_addc_u32 s7, s97, 0
	s_add_u32 s24, s96, 0x10a000
	s_addc_u32 s25, s97, 0
	s_lshl_b32 s0, s2, 13
	s_add_u32 s10, s4, s0
	s_addc_u32 s11, s5, 0
	s_add_u32 s12, s10, 0x1000
	s_addc_u32 s13, s11, 0
	s_lshl_b32 s0, s2, 12
	s_add_u32 s14, s6, s0
	s_addc_u32 s15, s7, 0
	s_lshr_b32 s0, s2, 12
	s_mul_i32 s0, s0, 0xc000
	s_add_u32 s16, s24, s0
	s_addc_u32 s17, s25, 0
	s_add_u32 s18, s16, 0x1000
	s_addc_u32 s19, s17, 0
	global_load_dwordx2 v[96:97], v225, s[14:15]
	global_load_dwordx2 v[98:99], v225, s[14:15] offset:512
	global_load_dwordx2 v[100:101], v225, s[14:15] offset:1024
	global_load_dwordx2 v[102:103], v225, s[14:15] offset:1536
	global_load_dwordx2 v[104:105], v225, s[14:15] offset:2048
	global_load_dwordx2 v[106:107], v225, s[14:15] offset:2560
	global_load_dwordx2 v[108:109], v225, s[14:15] offset:3072
	global_load_dwordx2 v[110:111], v225, s[14:15] offset:3584
	global_load_dword v64, v224, s[10:11] nt
	global_load_dword v65, v224, s[10:11] offset:2048 nt
	global_load_dword v66, v224, s[12:13] nt
	global_load_dword v67, v224, s[12:13] offset:2048 nt
	global_load_dword v68, v224, s[10:11] offset:256 nt
	global_load_dword v69, v224, s[10:11] offset:2304 nt
	global_load_dword v70, v224, s[12:13] offset:256 nt
	global_load_dword v71, v224, s[12:13] offset:2304 nt
	global_load_dword v72, v224, s[10:11] offset:512 nt
	global_load_dword v73, v224, s[10:11] offset:2560 nt
	global_load_dword v74, v224, s[12:13] offset:512 nt
	global_load_dword v75, v224, s[12:13] offset:2560 nt
	global_load_dword v76, v224, s[10:11] offset:768 nt
	global_load_dword v77, v224, s[10:11] offset:2816 nt
	global_load_dword v78, v224, s[12:13] offset:768 nt
	global_load_dword v79, v224, s[12:13] offset:2816 nt
	global_load_dword v80, v224, s[10:11] offset:1024 nt
	global_load_dword v81, v224, s[10:11] offset:3072 nt
	global_load_dword v82, v224, s[12:13] offset:1024 nt
	global_load_dword v83, v224, s[12:13] offset:3072 nt
	global_load_dword v84, v224, s[10:11] offset:1280 nt
	global_load_dword v85, v224, s[10:11] offset:3328 nt
	global_load_dword v86, v224, s[12:13] offset:1280 nt
	global_load_dword v87, v224, s[12:13] offset:3328 nt
	global_load_dword v88, v224, s[10:11] offset:1536 nt
	global_load_dword v89, v224, s[10:11] offset:3584 nt
	global_load_dword v90, v224, s[12:13] offset:1536 nt
	global_load_dword v91, v224, s[12:13] offset:3584 nt
	global_load_dword v92, v224, s[10:11] offset:1792 nt
	global_load_dword v93, v224, s[10:11] offset:3840 nt
	global_load_dword v94, v224, s[12:13] offset:1792 nt
	global_load_dword v95, v224, s[12:13] offset:3840 nt
	global_load_dwordx4 v[112:115], v226, s[16:17]
	global_load_dwordx4 v[116:119], v226, s[16:17] offset:1024
	global_load_dwordx4 v[120:123], v226, s[16:17] offset:2048
	global_load_dwordx4 v[124:127], v226, s[16:17] offset:3072
	global_load_dwordx4 v[128:131], v226, s[18:19]
	global_load_dwordx4 v[132:135], v226, s[18:19] offset:1024
	global_load_dwordx4 v[136:139], v226, s[18:19] offset:2048
	global_load_dwordx4 v[140:143], v226, s[18:19] offset:3072
	s_waitcnt vmcnt(0)
	s_branch .Lp9_ent_A

.Lp9_ent_A:
	s_add_i32 s3, s2, s9
	s_cmpk_lt_i32 s3, 0x2000
	s_cbranch_scc0 .Lp9_nold_A
	s_lshl_b32 s0, s3, 13
	s_add_u32 s10, s4, s0
	s_addc_u32 s11, s5, 0
	s_add_u32 s12, s10, 0x1000
	s_addc_u32 s13, s11, 0
	s_lshl_b32 s0, s3, 12
	s_add_u32 s14, s6, s0
	s_addc_u32 s15, s7, 0
	s_lshr_b32 s0, s3, 12
	s_mul_i32 s0, s0, 0xc000
	s_add_u32 s16, s24, s0
	s_addc_u32 s17, s25, 0
	s_add_u32 s18, s16, 0x1000
	s_addc_u32 s19, s17, 0
	global_load_dwordx2 v[176:177], v225, s[14:15]
	global_load_dwordx2 v[178:179], v225, s[14:15] offset:512
	global_load_dwordx2 v[180:181], v225, s[14:15] offset:1024
	global_load_dwordx2 v[182:183], v225, s[14:15] offset:1536
	global_load_dwordx2 v[184:185], v225, s[14:15] offset:2048
	global_load_dwordx2 v[186:187], v225, s[14:15] offset:2560
	global_load_dwordx2 v[188:189], v225, s[14:15] offset:3072
	global_load_dwordx2 v[190:191], v225, s[14:15] offset:3584
	global_load_dword v144, v224, s[10:11] nt
	global_load_dword v145, v224, s[10:11] offset:2048 nt
	global_load_dword v146, v224, s[12:13] nt
	global_load_dword v147, v224, s[12:13] offset:2048 nt
	global_load_dword v148, v224, s[10:11] offset:256 nt
	global_load_dword v149, v224, s[10:11] offset:2304 nt
	global_load_dword v150, v224, s[12:13] offset:256 nt
	global_load_dword v151, v224, s[12:13] offset:2304 nt
	global_load_dword v152, v224, s[10:11] offset:512 nt
	global_load_dword v153, v224, s[10:11] offset:2560 nt
	global_load_dword v154, v224, s[12:13] offset:512 nt
	global_load_dword v155, v224, s[12:13] offset:2560 nt
	global_load_dword v156, v224, s[10:11] offset:768 nt
	global_load_dword v157, v224, s[10:11] offset:2816 nt
	global_load_dword v158, v224, s[12:13] offset:768 nt
	global_load_dword v159, v224, s[12:13] offset:2816 nt
	global_load_dword v160, v224, s[10:11] offset:1024 nt
	global_load_dword v161, v224, s[10:11] offset:3072 nt
	global_load_dword v162, v224, s[12:13] offset:1024 nt
	global_load_dword v163, v224, s[12:13] offset:3072 nt
	global_load_dword v164, v224, s[10:11] offset:1280 nt
	global_load_dword v165, v224, s[10:11] offset:3328 nt
	global_load_dword v166, v224, s[12:13] offset:1280 nt
	global_load_dword v167, v224, s[12:13] offset:3328 nt
	global_load_dword v168, v224, s[10:11] offset:1536 nt
	global_load_dword v169, v224, s[10:11] offset:3584 nt
	global_load_dword v170, v224, s[12:13] offset:1536 nt
	global_load_dword v171, v224, s[12:13] offset:3584 nt
	global_load_dword v172, v224, s[10:11] offset:1792 nt
	global_load_dword v173, v224, s[10:11] offset:3840 nt
	global_load_dword v174, v224, s[12:13] offset:1792 nt
	global_load_dword v175, v224, s[12:13] offset:3840 nt
	global_load_dwordx4 v[192:195], v226, s[16:17]
	global_load_dwordx4 v[196:199], v226, s[16:17] offset:1024
	global_load_dwordx4 v[200:203], v226, s[16:17] offset:2048
	global_load_dwordx4 v[204:207], v226, s[16:17] offset:3072
	global_load_dwordx4 v[208:211], v226, s[18:19]
	global_load_dwordx4 v[212:215], v226, s[18:19] offset:1024
	global_load_dwordx4 v[216:219], v226, s[18:19] offset:2048
	global_load_dwordx4 v[220:223], v226, s[18:19] offset:3072
.Lp9_nold_A:
	v_cvt_pk_f32_fp8_e32 v[234:235], v64
	v_cvt_pk_f32_fp8_sdwa v[236:237], v64 src0_sel:WORD_1
	v_cvt_pk_f32_fp8_e32 v[238:239], v65
	v_cvt_pk_f32_fp8_sdwa v[240:241], v65 src0_sel:WORD_1
	v_lshlrev_b32_e32 v242, 16, v96
	v_and_b32_e32 v243, 0xffff0000, v96
	v_pk_add_f32 v[234:235], v[234:235], v[238:239]
	v_pk_add_f32 v[236:237], v[236:237], v[240:241]
	v_cvt_pk_f32_fp8_e32 v[238:239], v66
	v_cvt_pk_f32_fp8_sdwa v[240:241], v66 src0_sel:WORD_1
	v_lshlrev_b32_e32 v244, 16, v97
	v_and_b32_e32 v245, 0xffff0000, v97
	v_pk_add_f32 v[234:235], v[234:235], v[238:239]
	v_pk_add_f32 v[236:237], v[236:237], v[240:241]
	v_cvt_pk_f32_fp8_e32 v[238:239], v67
	v_cvt_pk_f32_fp8_sdwa v[240:241], v67 src0_sel:WORD_1
	v_pk_mul_f32 v[242:243], v[242:243], s[8:9] op_sel_hi:[1,0]
	v_pk_mul_f32 v[244:245], v[244:245], s[8:9] op_sel_hi:[1,0]
	v_pk_add_f32 v[234:235], v[234:235], v[238:239]
	v_pk_add_f32 v[236:237], v[236:237], v[240:241]
	v_pk_fma_f32 v[112:113], v[112:113], v[234:235], v[242:243]
	v_pk_fma_f32 v[114:115], v[114:115], v[236:237], v[244:245]
	v_pk_add_f32 v[246:247], v[112:113], v[114:115]
	v_cvt_pk_f32_fp8_e32 v[234:235], v68
	v_cvt_pk_f32_fp8_sdwa v[236:237], v68 src0_sel:WORD_1
	v_cvt_pk_f32_fp8_e32 v[238:239], v69
	v_cvt_pk_f32_fp8_sdwa v[240:241], v69 src0_sel:WORD_1
	v_lshlrev_b32_e32 v242, 16, v98
	v_and_b32_e32 v243, 0xffff0000, v98
	v_pk_add_f32 v[234:235], v[234:235], v[238:239]
	v_pk_add_f32 v[236:237], v[236:237], v[240:241]
	v_cvt_pk_f32_fp8_e32 v[238:239], v70
	v_cvt_pk_f32_fp8_sdwa v[240:241], v70 src0_sel:WORD_1
	v_lshlrev_b32_e32 v244, 16, v99
	v_and_b32_e32 v245, 0xffff0000, v99
	v_pk_add_f32 v[234:235], v[234:235], v[238:239]
	v_pk_add_f32 v[236:237], v[236:237], v[240:241]
	v_cvt_pk_f32_fp8_e32 v[238:239], v71
	v_cvt_pk_f32_fp8_sdwa v[240:241], v71 src0_sel:WORD_1
	v_pk_mul_f32 v[242:243], v[242:243], s[8:9] op_sel_hi:[1,0]
	v_pk_mul_f32 v[244:245], v[244:245], s[8:9] op_sel_hi:[1,0]
	v_pk_add_f32 v[234:235], v[234:235], v[238:239]
	v_pk_add_f32 v[236:237], v[236:237], v[240:241]
	v_pk_fma_f32 v[116:117], v[116:117], v[234:235], v[242:243]
	v_pk_fma_f32 v[118:119], v[118:119], v[236:237], v[244:245]
	v_pk_add_f32 v[246:247], v[246:247], v[116:117]
	v_pk_add_f32 v[246:247], v[246:247], v[118:119]
	v_cvt_pk_f32_fp8_e32 v[234:235], v72
	v_cvt_pk_f32_fp8_sdwa v[236:237], v72 src0_sel:WORD_1
	v_cvt_pk_f32_fp8_e32 v[238:239], v73
	v_cvt_pk_f32_fp8_sdwa v[240:241], v73 src0_sel:WORD_1
	v_lshlrev_b32_e32 v242, 16, v100
	v_and_b32_e32 v243, 0xffff0000, v100
	v_pk_add_f32 v[234:235], v[234:235], v[238:239]
	v_pk_add_f32 v[236:237], v[236:237], v[240:241]
	v_cvt_pk_f32_fp8_e32 v[238:239], v74
	v_cvt_pk_f32_fp8_sdwa v[240:241], v74 src0_sel:WORD_1
	v_lshlrev_b32_e32 v244, 16, v101
	v_and_b32_e32 v245, 0xffff0000, v101
	v_pk_add_f32 v[234:235], v[234:235], v[238:239]
	v_pk_add_f32 v[236:237], v[236:237], v[240:241]
	v_cvt_pk_f32_fp8_e32 v[238:239], v75
	v_cvt_pk_f32_fp8_sdwa v[240:241], v75 src0_sel:WORD_1
	v_pk_mul_f32 v[242:243], v[242:243], s[8:9] op_sel_hi:[1,0]
	v_pk_mul_f32 v[244:245], v[244:245], s[8:9] op_sel_hi:[1,0]
	v_pk_add_f32 v[234:235], v[234:235], v[238:239]
	v_pk_add_f32 v[236:237], v[236:237], v[240:241]
	v_pk_fma_f32 v[120:121], v[120:121], v[234:235], v[242:243]
	v_pk_fma_f32 v[122:123], v[122:123], v[236:237], v[244:245]
	v_pk_add_f32 v[246:247], v[246:247], v[120:121]
	v_pk_add_f32 v[246:247], v[246:247], v[122:123]
	v_cvt_pk_f32_fp8_e32 v[234:235], v76
	v_cvt_pk_f32_fp8_sdwa v[236:237], v76 src0_sel:WORD_1
	v_cvt_pk_f32_fp8_e32 v[238:239], v77
	v_cvt_pk_f32_fp8_sdwa v[240:241], v77 src0_sel:WORD_1
	v_lshlrev_b32_e32 v242, 16, v102
	v_and_b32_e32 v243, 0xffff0000, v102
	v_pk_add_f32 v[234:235], v[234:235], v[238:239]
	v_pk_add_f32 v[236:237], v[236:237], v[240:241]
	v_cvt_pk_f32_fp8_e32 v[238:239], v78
	v_cvt_pk_f32_fp8_sdwa v[240:241], v78 src0_sel:WORD_1
	v_lshlrev_b32_e32 v244, 16, v103
	v_and_b32_e32 v245, 0xffff0000, v103
	v_pk_add_f32 v[234:235], v[234:235], v[238:239]
	v_pk_add_f32 v[236:237], v[236:237], v[240:241]
	v_cvt_pk_f32_fp8_e32 v[238:239], v79
	v_cvt_pk_f32_fp8_sdwa v[240:241], v79 src0_sel:WORD_1
	v_pk_mul_f32 v[242:243], v[242:243], s[8:9] op_sel_hi:[1,0]
	v_pk_mul_f32 v[244:245], v[244:245], s[8:9] op_sel_hi:[1,0]
	v_pk_add_f32 v[234:235], v[234:235], v[238:239]
	v_pk_add_f32 v[236:237], v[236:237], v[240:241]
	v_pk_fma_f32 v[124:125], v[124:125], v[234:235], v[242:243]
	v_pk_fma_f32 v[126:127], v[126:127], v[236:237], v[244:245]
	v_pk_add_f32 v[246:247], v[246:247], v[124:125]
	v_pk_add_f32 v[246:247], v[246:247], v[126:127]
	v_cvt_pk_f32_fp8_e32 v[234:235], v80
	v_cvt_pk_f32_fp8_sdwa v[236:237], v80 src0_sel:WORD_1
	v_cvt_pk_f32_fp8_e32 v[238:239], v81
	v_cvt_pk_f32_fp8_sdwa v[240:241], v81 src0_sel:WORD_1
	v_lshlrev_b32_e32 v242, 16, v104
	v_and_b32_e32 v243, 0xffff0000, v104
	v_pk_add_f32 v[234:235], v[234:235], v[238:239]
	v_pk_add_f32 v[236:237], v[236:237], v[240:241]
	v_cvt_pk_f32_fp8_e32 v[238:239], v82
	v_cvt_pk_f32_fp8_sdwa v[240:241], v82 src0_sel:WORD_1
	v_lshlrev_b32_e32 v244, 16, v105
	v_and_b32_e32 v245, 0xffff0000, v105
	v_pk_add_f32 v[234:235], v[234:235], v[238:239]
	v_pk_add_f32 v[236:237], v[236:237], v[240:241]
	v_cvt_pk_f32_fp8_e32 v[238:239], v83
	v_cvt_pk_f32_fp8_sdwa v[240:241], v83 src0_sel:WORD_1
	v_pk_mul_f32 v[242:243], v[242:243], s[8:9] op_sel_hi:[1,0]
	v_pk_mul_f32 v[244:245], v[244:245], s[8:9] op_sel_hi:[1,0]
	v_pk_add_f32 v[234:235], v[234:235], v[238:239]
	v_pk_add_f32 v[236:237], v[236:237], v[240:241]
	v_pk_fma_f32 v[128:129], v[128:129], v[234:235], v[242:243]
	v_pk_fma_f32 v[130:131], v[130:131], v[236:237], v[244:245]
	v_pk_add_f32 v[246:247], v[246:247], v[128:129]
	v_pk_add_f32 v[246:247], v[246:247], v[130:131]
	v_cvt_pk_f32_fp8_e32 v[234:235], v84
	v_cvt_pk_f32_fp8_sdwa v[236:237], v84 src0_sel:WORD_1
	v_cvt_pk_f32_fp8_e32 v[238:239], v85
	v_cvt_pk_f32_fp8_sdwa v[240:241], v85 src0_sel:WORD_1
	v_lshlrev_b32_e32 v242, 16, v106
	v_and_b32_e32 v243, 0xffff0000, v106
	v_pk_add_f32 v[234:235], v[234:235], v[238:239]
	v_pk_add_f32 v[236:237], v[236:237], v[240:241]
	v_cvt_pk_f32_fp8_e32 v[238:239], v86
	v_cvt_pk_f32_fp8_sdwa v[240:241], v86 src0_sel:WORD_1
	v_lshlrev_b32_e32 v244, 16, v107
	v_and_b32_e32 v245, 0xffff0000, v107
	v_pk_add_f32 v[234:235], v[234:235], v[238:239]
	v_pk_add_f32 v[236:237], v[236:237], v[240:241]
	v_cvt_pk_f32_fp8_e32 v[238:239], v87
	v_cvt_pk_f32_fp8_sdwa v[240:241], v87 src0_sel:WORD_1
	v_pk_mul_f32 v[242:243], v[242:243], s[8:9] op_sel_hi:[1,0]
	v_pk_mul_f32 v[244:245], v[244:245], s[8:9] op_sel_hi:[1,0]
	v_pk_add_f32 v[234:235], v[234:235], v[238:239]
	v_pk_add_f32 v[236:237], v[236:237], v[240:241]
	v_pk_fma_f32 v[132:133], v[132:133], v[234:235], v[242:243]
	v_pk_fma_f32 v[134:135], v[134:135], v[236:237], v[244:245]
	v_pk_add_f32 v[246:247], v[246:247], v[132:133]
	v_pk_add_f32 v[246:247], v[246:247], v[134:135]
	v_cvt_pk_f32_fp8_e32 v[234:235], v88
	v_cvt_pk_f32_fp8_sdwa v[236:237], v88 src0_sel:WORD_1
	v_cvt_pk_f32_fp8_e32 v[238:239], v89
	v_cvt_pk_f32_fp8_sdwa v[240:241], v89 src0_sel:WORD_1
	v_lshlrev_b32_e32 v242, 16, v108
	v_and_b32_e32 v243, 0xffff0000, v108
	v_pk_add_f32 v[234:235], v[234:235], v[238:239]
	v_pk_add_f32 v[236:237], v[236:237], v[240:241]
	v_cvt_pk_f32_fp8_e32 v[238:239], v90
	v_cvt_pk_f32_fp8_sdwa v[240:241], v90 src0_sel:WORD_1
	v_lshlrev_b32_e32 v244, 16, v109
	v_and_b32_e32 v245, 0xffff0000, v109
	v_pk_add_f32 v[234:235], v[234:235], v[238:239]
	v_pk_add_f32 v[236:237], v[236:237], v[240:241]
	v_cvt_pk_f32_fp8_e32 v[238:239], v91
	v_cvt_pk_f32_fp8_sdwa v[240:241], v91 src0_sel:WORD_1
	v_pk_mul_f32 v[242:243], v[242:243], s[8:9] op_sel_hi:[1,0]
	v_pk_mul_f32 v[244:245], v[244:245], s[8:9] op_sel_hi:[1,0]
	v_pk_add_f32 v[234:235], v[234:235], v[238:239]
	v_pk_add_f32 v[236:237], v[236:237], v[240:241]
	v_pk_fma_f32 v[136:137], v[136:137], v[234:235], v[242:243]
	v_pk_fma_f32 v[138:139], v[138:139], v[236:237], v[244:245]
	v_pk_add_f32 v[246:247], v[246:247], v[136:137]
	v_pk_add_f32 v[246:247], v[246:247], v[138:139]
	v_cvt_pk_f32_fp8_e32 v[234:235], v92
	v_cvt_pk_f32_fp8_sdwa v[236:237], v92 src0_sel:WORD_1
	v_cvt_pk_f32_fp8_e32 v[238:239], v93
	v_cvt_pk_f32_fp8_sdwa v[240:241], v93 src0_sel:WORD_1
	v_lshlrev_b32_e32 v242, 16, v110
	v_and_b32_e32 v243, 0xffff0000, v110
	v_pk_add_f32 v[234:235], v[234:235], v[238:239]
	v_pk_add_f32 v[236:237], v[236:237], v[240:241]
	v_cvt_pk_f32_fp8_e32 v[238:239], v94
	v_cvt_pk_f32_fp8_sdwa v[240:241], v94 src0_sel:WORD_1
	v_lshlrev_b32_e32 v244, 16, v111
	v_and_b32_e32 v245, 0xffff0000, v111
	v_pk_add_f32 v[234:235], v[234:235], v[238:239]
	v_pk_add_f32 v[236:237], v[236:237], v[240:241]
	v_cvt_pk_f32_fp8_e32 v[238:239], v95
	v_cvt_pk_f32_fp8_sdwa v[240:241], v95 src0_sel:WORD_1
	v_pk_mul_f32 v[242:243], v[242:243], s[8:9] op_sel_hi:[1,0]
	v_pk_mul_f32 v[244:245], v[244:245], s[8:9] op_sel_hi:[1,0]
	v_pk_add_f32 v[234:235], v[234:235], v[238:239]
	v_pk_add_f32 v[236:237], v[236:237], v[240:241]
	v_pk_fma_f32 v[140:141], v[140:141], v[234:235], v[242:243]
	v_pk_fma_f32 v[142:143], v[142:143], v[236:237], v[244:245]
	v_pk_add_f32 v[246:247], v[246:247], v[140:141]
	v_pk_add_f32 v[246:247], v[246:247], v[142:143]
	v_add_f32_e32 v246, v246, v247
	ds_bpermute_b32 v248, v228, v246
	s_waitcnt lgkmcnt(0)
	v_add_f32_e32 v246, v246, v248
	ds_bpermute_b32 v248, v229, v246
	s_waitcnt lgkmcnt(0)
	v_add_f32_e32 v246, v246, v248
	ds_bpermute_b32 v248, v230, v246
	s_waitcnt lgkmcnt(0)
	v_add_f32_e32 v246, v246, v248
	ds_bpermute_b32 v248, v231, v246
	s_waitcnt lgkmcnt(0)
	v_add_f32_e32 v246, v246, v248
	ds_bpermute_b32 v248, v232, v246
	s_waitcnt lgkmcnt(0)
	v_add_f32_e32 v246, v246, v248
	ds_bpermute_b32 v248, v233, v246
	s_waitcnt lgkmcnt(0)
	v_add_f32_e32 v246, v246, v248
	v_mul_f32_e32 v248, 0xba000000, v246
	v_pk_add_f32 v[112:113], v[112:113], v[248:249] op_sel_hi:[1,0]
	v_pk_add_f32 v[114:115], v[114:115], v[248:249] op_sel_hi:[1,0]
	v_pk_add_f32 v[116:117], v[116:117], v[248:249] op_sel_hi:[1,0]
	v_pk_add_f32 v[118:119], v[118:119], v[248:249] op_sel_hi:[1,0]
	v_pk_add_f32 v[120:121], v[120:121], v[248:249] op_sel_hi:[1,0]
	v_pk_add_f32 v[122:123], v[122:123], v[248:249] op_sel_hi:[1,0]
	v_pk_add_f32 v[124:125], v[124:125], v[248:249] op_sel_hi:[1,0]
	v_pk_add_f32 v[126:127], v[126:127], v[248:249] op_sel_hi:[1,0]
	v_pk_add_f32 v[128:129], v[128:129], v[248:249] op_sel_hi:[1,0]
	v_pk_add_f32 v[130:131], v[130:131], v[248:249] op_sel_hi:[1,0]
	v_pk_add_f32 v[132:133], v[132:133], v[248:249] op_sel_hi:[1,0]
	v_pk_add_f32 v[134:135], v[134:135], v[248:249] op_sel_hi:[1,0]
	v_pk_add_f32 v[136:137], v[136:137], v[248:249] op_sel_hi:[1,0]
	v_pk_add_f32 v[138:139], v[138:139], v[248:249] op_sel_hi:[1,0]
	v_pk_add_f32 v[140:141], v[140:141], v[248:249] op_sel_hi:[1,0]
	v_pk_add_f32 v[142:143], v[142:143], v[248:249] op_sel_hi:[1,0]
	v_pk_mul_f32 v[250:251], v[112:113], v[112:113]
	v_pk_fma_f32 v[250:251], v[114:115], v[114:115], v[250:251]
	v_pk_fma_f32 v[250:251], v[116:117], v[116:117], v[250:251]
	v_pk_fma_f32 v[250:251], v[118:119], v[118:119], v[250:251]
	v_pk_fma_f32 v[250:251], v[120:121], v[120:121], v[250:251]
	v_pk_fma_f32 v[250:251], v[122:123], v[122:123], v[250:251]
	v_pk_fma_f32 v[250:251], v[124:125], v[124:125], v[250:251]
	v_pk_fma_f32 v[250:251], v[126:127], v[126:127], v[250:251]
	v_pk_fma_f32 v[250:251], v[128:129], v[128:129], v[250:251]
	v_pk_fma_f32 v[250:251], v[130:131], v[130:131], v[250:251]
	v_pk_fma_f32 v[250:251], v[132:133], v[132:133], v[250:251]
	v_pk_fma_f32 v[250:251], v[134:135], v[134:135], v[250:251]
	v_pk_fma_f32 v[250:251], v[136:137], v[136:137], v[250:251]
	v_pk_fma_f32 v[250:251], v[138:139], v[138:139], v[250:251]
	v_pk_fma_f32 v[250:251], v[140:141], v[140:141], v[250:251]
	v_pk_fma_f32 v[250:251], v[142:143], v[142:143], v[250:251]
	v_add_f32_e32 v250, v250, v251
	ds_bpermute_b32 v248, v228, v250
	s_waitcnt lgkmcnt(0)
	v_add_f32_e32 v250, v250, v248
	ds_bpermute_b32 v248, v229, v250
	s_waitcnt lgkmcnt(0)
	v_add_f32_e32 v250, v250, v248
	ds_bpermute_b32 v248, v230, v250
	s_waitcnt lgkmcnt(0)
	v_add_f32_e32 v250, v250, v248
	ds_bpermute_b32 v248, v231, v250
	s_waitcnt lgkmcnt(0)
	v_add_f32_e32 v250, v250, v248
	ds_bpermute_b32 v248, v232, v250
	s_waitcnt lgkmcnt(0)
	v_add_f32_e32 v250, v250, v248
	ds_bpermute_b32 v248, v233, v250
	s_waitcnt lgkmcnt(0)
	v_add_f32_e32 v250, v250, v248
	v_mul_f32_e32 v234, 0x3a000000, v250
	v_add_f32_e32 v234, 0x3727c5ac, v234
	v_mul_f32_e32 v235, 0x4f800000, v234
	v_cmp_gt_f32_e32 vcc, s23, v234
	s_nop 1
	v_cndmask_b32_e32 v234, v234, v235, vcc
	v_sqrt_f32_e32 v235, v234
	s_nop 0
	v_add_u32_e32 v236, -1, v235
	v_add_u32_e32 v237, 1, v235
	v_fma_f32 v238, -v236, v235, v234
	v_fma_f32 v239, -v237, v235, v234
	v_cmp_ge_f32_e64 s[0:1], 0, v238
	s_nop 1
	v_cndmask_b32_e64 v235, v235, v236, s[0:1]
	v_cmp_lt_f32_e64 s[0:1], 0, v239
	s_nop 1
	v_cndmask_b32_e64 v235, v235, v237, s[0:1]
	v_mul_f32_e32 v236, 0x37800000, v235
	v_cndmask_b32_e32 v235, v235, v236, vcc
	v_cmp_class_f32_e64 vcc, v234, s22
	s_nop 1
	v_cndmask_b32_e32 v234, v235, v234, vcc
	v_div_scale_f32 v235, s[0:1], v234, v234, 1.0
	v_rcp_f32_e32 v237, v235
	v_div_scale_f32 v236, vcc, 1.0, v234, 1.0
	v_fma_f32 v238, -v235, v237, 1.0
	v_fmac_f32_e32 v237, v238, v237
	v_mul_f32_e32 v238, v236, v237
	v_fma_f32 v239, -v235, v238, v236
	v_fmac_f32_e32 v238, v239, v237
	v_fma_f32 v235, -v235, v238, v236
	v_div_fmas_f32 v235, v235, v237, v238
	v_div_fixup_f32 v234, v235, v234, 1.0
	v_pk_mul_f32 v[112:113], v[112:113], v[234:235] op_sel_hi:[1,0]
	v_pk_mul_f32 v[114:115], v[114:115], v[234:235] op_sel_hi:[1,0]
	v_pk_mul_f32 v[116:117], v[116:117], v[234:235] op_sel_hi:[1,0]
	v_pk_mul_f32 v[118:119], v[118:119], v[234:235] op_sel_hi:[1,0]
	v_pk_mul_f32 v[120:121], v[120:121], v[234:235] op_sel_hi:[1,0]
	v_pk_mul_f32 v[122:123], v[122:123], v[234:235] op_sel_hi:[1,0]
	v_pk_mul_f32 v[124:125], v[124:125], v[234:235] op_sel_hi:[1,0]
	v_pk_mul_f32 v[126:127], v[126:127], v[234:235] op_sel_hi:[1,0]
	v_pk_mul_f32 v[128:129], v[128:129], v[234:235] op_sel_hi:[1,0]
	v_pk_mul_f32 v[130:131], v[130:131], v[234:235] op_sel_hi:[1,0]
	v_pk_mul_f32 v[132:133], v[132:133], v[234:235] op_sel_hi:[1,0]
	v_pk_mul_f32 v[134:135], v[134:135], v[234:235] op_sel_hi:[1,0]
	v_pk_mul_f32 v[136:137], v[136:137], v[234:235] op_sel_hi:[1,0]
	v_pk_mul_f32 v[138:139], v[138:139], v[234:235] op_sel_hi:[1,0]
	v_pk_mul_f32 v[140:141], v[140:141], v[234:235] op_sel_hi:[1,0]
	v_pk_mul_f32 v[142:143], v[142:143], v[234:235] op_sel_hi:[1,0]
	v_pk_fma_f32 v[112:113], v[20:21], v[112:113], v[0:1]
	v_pk_fma_f32 v[114:115], v[22:23], v[114:115], v[2:3]
	v_pk_fma_f32 v[116:117], v[24:25], v[116:117], v[4:5]
	v_pk_fma_f32 v[118:119], v[26:27], v[118:119], v[6:7]
	v_pk_fma_f32 v[120:121], v[32:33], v[120:121], v[8:9]
	v_pk_fma_f32 v[122:123], v[34:35], v[122:123], v[10:11]
	v_pk_fma_f32 v[124:125], v[40:41], v[124:125], v[12:13]
	v_pk_fma_f32 v[126:127], v[42:43], v[126:127], v[14:15]
	v_pk_fma_f32 v[128:129], v[52:53], v[128:129], v[28:29]
	v_pk_fma_f32 v[130:131], v[54:55], v[130:131], v[30:31]
	v_pk_fma_f32 v[132:133], v[56:57], v[132:133], v[36:37]
	v_pk_fma_f32 v[134:135], v[58:59], v[134:135], v[38:39]
	v_pk_fma_f32 v[136:137], v[60:61], v[136:137], v[44:45]
	v_pk_fma_f32 v[138:139], v[62:63], v[138:139], v[46:47]
	v_pk_fma_f32 v[140:141], v[48:49], v[140:141], v[16:17]
	v_pk_fma_f32 v[142:143], v[50:51], v[142:143], v[18:19]
	s_lshl_b32 s0, s2, 13
	s_add_u32 s20, s26, s0
	s_addc_u32 s21, s27, 0
	global_store_dwordx4 v226, v[112:115], s[20:21] nt
	global_store_dwordx4 v226, v[116:119], s[20:21] offset:1024 nt
	global_store_dwordx4 v226, v[120:123], s[20:21] offset:2048 nt
	global_store_dwordx4 v226, v[124:127], s[20:21] offset:3072 nt
	global_store_dwordx4 v227, v[128:131], s[20:21] nt
	global_store_dwordx4 v227, v[132:135], s[20:21] offset:1024 nt
	global_store_dwordx4 v227, v[136:139], s[20:21] offset:2048 nt
	global_store_dwordx4 v227, v[140:143], s[20:21] offset:3072 nt
	s_mov_b32 s2, s3
	s_cmpk_lt_i32 s2, 0x2000
	s_cbranch_scc0 .LBB0_1225

.Lp9_ent_B:
	s_add_i32 s3, s2, s9
	s_cmpk_lt_i32 s3, 0x2000
	s_cbranch_scc0 .Lp9_nold_B
	s_lshl_b32 s0, s3, 13
	s_add_u32 s10, s4, s0
	s_addc_u32 s11, s5, 0
	s_add_u32 s12, s10, 0x1000
	s_addc_u32 s13, s11, 0
	s_lshl_b32 s0, s3, 12
	s_add_u32 s14, s6, s0
	s_addc_u32 s15, s7, 0
	s_lshr_b32 s0, s3, 12
	s_mul_i32 s0, s0, 0xc000
	s_add_u32 s16, s24, s0
	s_addc_u32 s17, s25, 0
	s_add_u32 s18, s16, 0x1000
	s_addc_u32 s19, s17, 0
	global_load_dwordx2 v[96:97], v225, s[14:15]
	global_load_dwordx2 v[98:99], v225, s[14:15] offset:512
	global_load_dwordx2 v[100:101], v225, s[14:15] offset:1024
	global_load_dwordx2 v[102:103], v225, s[14:15] offset:1536
	global_load_dwordx2 v[104:105], v225, s[14:15] offset:2048
	global_load_dwordx2 v[106:107], v225, s[14:15] offset:2560
	global_load_dwordx2 v[108:109], v225, s[14:15] offset:3072
	global_load_dwordx2 v[110:111], v225, s[14:15] offset:3584
	global_load_dword v64, v224, s[10:11] nt
	global_load_dword v65, v224, s[10:11] offset:2048 nt
	global_load_dword v66, v224, s[12:13] nt
	global_load_dword v67, v224, s[12:13] offset:2048 nt
	global_load_dword v68, v224, s[10:11] offset:256 nt
	global_load_dword v69, v224, s[10:11] offset:2304 nt
	global_load_dword v70, v224, s[12:13] offset:256 nt
	global_load_dword v71, v224, s[12:13] offset:2304 nt
	global_load_dword v72, v224, s[10:11] offset:512 nt
	global_load_dword v73, v224, s[10:11] offset:2560 nt
	global_load_dword v74, v224, s[12:13] offset:512 nt
	global_load_dword v75, v224, s[12:13] offset:2560 nt
	global_load_dword v76, v224, s[10:11] offset:768 nt
	global_load_dword v77, v224, s[10:11] offset:2816 nt
	global_load_dword v78, v224, s[12:13] offset:768 nt
	global_load_dword v79, v224, s[12:13] offset:2816 nt
	global_load_dword v80, v224, s[10:11] offset:1024 nt
	global_load_dword v81, v224, s[10:11] offset:3072 nt
	global_load_dword v82, v224, s[12:13] offset:1024 nt
	global_load_dword v83, v224, s[12:13] offset:3072 nt
	global_load_dword v84, v224, s[10:11] offset:1280 nt
	global_load_dword v85, v224, s[10:11] offset:3328 nt
	global_load_dword v86, v224, s[12:13] offset:1280 nt
	global_load_dword v87, v224, s[12:13] offset:3328 nt
	global_load_dword v88, v224, s[10:11] offset:1536 nt
	global_load_dword v89, v224, s[10:11] offset:3584 nt
	global_load_dword v90, v224, s[12:13] offset:1536 nt
	global_load_dword v91, v224, s[12:13] offset:3584 nt
	global_load_dword v92, v224, s[10:11] offset:1792 nt
	global_load_dword v93, v224, s[10:11] offset:3840 nt
	global_load_dword v94, v224, s[12:13] offset:1792 nt
	global_load_dword v95, v224, s[12:13] offset:3840 nt
	global_load_dwordx4 v[112:115], v226, s[16:17]
	global_load_dwordx4 v[116:119], v226, s[16:17] offset:1024
	global_load_dwordx4 v[120:123], v226, s[16:17] offset:2048
	global_load_dwordx4 v[124:127], v226, s[16:17] offset:3072
	global_load_dwordx4 v[128:131], v226, s[18:19]
	global_load_dwordx4 v[132:135], v226, s[18:19] offset:1024
	global_load_dwordx4 v[136:139], v226, s[18:19] offset:2048
	global_load_dwordx4 v[140:143], v226, s[18:19] offset:3072
.Lp9_nold_B:
	v_cvt_pk_f32_fp8_e32 v[234:235], v144
	v_cvt_pk_f32_fp8_sdwa v[236:237], v144 src0_sel:WORD_1
	v_cvt_pk_f32_fp8_e32 v[238:239], v145
	v_cvt_pk_f32_fp8_sdwa v[240:241], v145 src0_sel:WORD_1
	v_lshlrev_b32_e32 v242, 16, v176
	v_and_b32_e32 v243, 0xffff0000, v176
	v_pk_add_f32 v[234:235], v[234:235], v[238:239]
	v_pk_add_f32 v[236:237], v[236:237], v[240:241]
	v_cvt_pk_f32_fp8_e32 v[238:239], v146
	v_cvt_pk_f32_fp8_sdwa v[240:241], v146 src0_sel:WORD_1
	v_lshlrev_b32_e32 v244, 16, v177
	v_and_b32_e32 v245, 0xffff0000, v177
	v_pk_add_f32 v[234:235], v[234:235], v[238:239]
	v_pk_add_f32 v[236:237], v[236:237], v[240:241]
	v_cvt_pk_f32_fp8_e32 v[238:239], v147
	v_cvt_pk_f32_fp8_sdwa v[240:241], v147 src0_sel:WORD_1
	v_pk_mul_f32 v[242:243], v[242:243], s[8:9] op_sel_hi:[1,0]
	v_pk_mul_f32 v[244:245], v[244:245], s[8:9] op_sel_hi:[1,0]
	v_pk_add_f32 v[234:235], v[234:235], v[238:239]
	v_pk_add_f32 v[236:237], v[236:237], v[240:241]
	v_pk_fma_f32 v[192:193], v[192:193], v[234:235], v[242:243]
	v_pk_fma_f32 v[194:195], v[194:195], v[236:237], v[244:245]
	v_pk_add_f32 v[246:247], v[192:193], v[194:195]
	v_cvt_pk_f32_fp8_e32 v[234:235], v148
	v_cvt_pk_f32_fp8_sdwa v[236:237], v148 src0_sel:WORD_1
	v_cvt_pk_f32_fp8_e32 v[238:239], v149
	v_cvt_pk_f32_fp8_sdwa v[240:241], v149 src0_sel:WORD_1
	v_lshlrev_b32_e32 v242, 16, v178
	v_and_b32_e32 v243, 0xffff0000, v178
	v_pk_add_f32 v[234:235], v[234:235], v[238:239]
	v_pk_add_f32 v[236:237], v[236:237], v[240:241]
	v_cvt_pk_f32_fp8_e32 v[238:239], v150
	v_cvt_pk_f32_fp8_sdwa v[240:241], v150 src0_sel:WORD_1
	v_lshlrev_b32_e32 v244, 16, v179
	v_and_b32_e32 v245, 0xffff0000, v179
	v_pk_add_f32 v[234:235], v[234:235], v[238:239]
	v_pk_add_f32 v[236:237], v[236:237], v[240:241]
	v_cvt_pk_f32_fp8_e32 v[238:239], v151
	v_cvt_pk_f32_fp8_sdwa v[240:241], v151 src0_sel:WORD_1
	v_pk_mul_f32 v[242:243], v[242:243], s[8:9] op_sel_hi:[1,0]
	v_pk_mul_f32 v[244:245], v[244:245], s[8:9] op_sel_hi:[1,0]
	v_pk_add_f32 v[234:235], v[234:235], v[238:239]
	v_pk_add_f32 v[236:237], v[236:237], v[240:241]
	v_pk_fma_f32 v[196:197], v[196:197], v[234:235], v[242:243]
	v_pk_fma_f32 v[198:199], v[198:199], v[236:237], v[244:245]
	v_pk_add_f32 v[246:247], v[246:247], v[196:197]
	v_pk_add_f32 v[246:247], v[246:247], v[198:199]
	v_cvt_pk_f32_fp8_e32 v[234:235], v152
	v_cvt_pk_f32_fp8_sdwa v[236:237], v152 src0_sel:WORD_1
	v_cvt_pk_f32_fp8_e32 v[238:239], v153
	v_cvt_pk_f32_fp8_sdwa v[240:241], v153 src0_sel:WORD_1
	v_lshlrev_b32_e32 v242, 16, v180
	v_and_b32_e32 v243, 0xffff0000, v180
	v_pk_add_f32 v[234:235], v[234:235], v[238:239]
	v_pk_add_f32 v[236:237], v[236:237], v[240:241]
	v_cvt_pk_f32_fp8_e32 v[238:239], v154
	v_cvt_pk_f32_fp8_sdwa v[240:241], v154 src0_sel:WORD_1
	v_lshlrev_b32_e32 v244, 16, v181
	v_and_b32_e32 v245, 0xffff0000, v181
	v_pk_add_f32 v[234:235], v[234:235], v[238:239]
	v_pk_add_f32 v[236:237], v[236:237], v[240:241]
	v_cvt_pk_f32_fp8_e32 v[238:239], v155
	v_cvt_pk_f32_fp8_sdwa v[240:241], v155 src0_sel:WORD_1
	v_pk_mul_f32 v[242:243], v[242:243], s[8:9] op_sel_hi:[1,0]
	v_pk_mul_f32 v[244:245], v[244:245], s[8:9] op_sel_hi:[1,0]
	v_pk_add_f32 v[234:235], v[234:235], v[238:239]
	v_pk_add_f32 v[236:237], v[236:237], v[240:241]
	v_pk_fma_f32 v[200:201], v[200:201], v[234:235], v[242:243]
	v_pk_fma_f32 v[202:203], v[202:203], v[236:237], v[244:245]
	v_pk_add_f32 v[246:247], v[246:247], v[200:201]
	v_pk_add_f32 v[246:247], v[246:247], v[202:203]
	v_cvt_pk_f32_fp8_e32 v[234:235], v156
	v_cvt_pk_f32_fp8_sdwa v[236:237], v156 src0_sel:WORD_1
	v_cvt_pk_f32_fp8_e32 v[238:239], v157
	v_cvt_pk_f32_fp8_sdwa v[240:241], v157 src0_sel:WORD_1
	v_lshlrev_b32_e32 v242, 16, v182
	v_and_b32_e32 v243, 0xffff0000, v182
	v_pk_add_f32 v[234:235], v[234:235], v[238:239]
	v_pk_add_f32 v[236:237], v[236:237], v[240:241]
	v_cvt_pk_f32_fp8_e32 v[238:239], v158
	v_cvt_pk_f32_fp8_sdwa v[240:241], v158 src0_sel:WORD_1
	v_lshlrev_b32_e32 v244, 16, v183
	v_and_b32_e32 v245, 0xffff0000, v183
	v_pk_add_f32 v[234:235], v[234:235], v[238:239]
	v_pk_add_f32 v[236:237], v[236:237], v[240:241]
	v_cvt_pk_f32_fp8_e32 v[238:239], v159
	v_cvt_pk_f32_fp8_sdwa v[240:241], v159 src0_sel:WORD_1
	v_pk_mul_f32 v[242:243], v[242:243], s[8:9] op_sel_hi:[1,0]
	v_pk_mul_f32 v[244:245], v[244:245], s[8:9] op_sel_hi:[1,0]
	v_pk_add_f32 v[234:235], v[234:235], v[238:239]
	v_pk_add_f32 v[236:237], v[236:237], v[240:241]
	v_pk_fma_f32 v[204:205], v[204:205], v[234:235], v[242:243]
	v_pk_fma_f32 v[206:207], v[206:207], v[236:237], v[244:245]
	v_pk_add_f32 v[246:247], v[246:247], v[204:205]
	v_pk_add_f32 v[246:247], v[246:247], v[206:207]
	v_cvt_pk_f32_fp8_e32 v[234:235], v160
	v_cvt_pk_f32_fp8_sdwa v[236:237], v160 src0_sel:WORD_1
	v_cvt_pk_f32_fp8_e32 v[238:239], v161
	v_cvt_pk_f32_fp8_sdwa v[240:241], v161 src0_sel:WORD_1
	v_lshlrev_b32_e32 v242, 16, v184
	v_and_b32_e32 v243, 0xffff0000, v184
	v_pk_add_f32 v[234:235], v[234:235], v[238:239]
	v_pk_add_f32 v[236:237], v[236:237], v[240:241]
	v_cvt_pk_f32_fp8_e32 v[238:239], v162
	v_cvt_pk_f32_fp8_sdwa v[240:241], v162 src0_sel:WORD_1
	v_lshlrev_b32_e32 v244, 16, v185
	v_and_b32_e32 v245, 0xffff0000, v185
	v_pk_add_f32 v[234:235], v[234:235], v[238:239]
	v_pk_add_f32 v[236:237], v[236:237], v[240:241]
	v_cvt_pk_f32_fp8_e32 v[238:239], v163
	v_cvt_pk_f32_fp8_sdwa v[240:241], v163 src0_sel:WORD_1
	v_pk_mul_f32 v[242:243], v[242:243], s[8:9] op_sel_hi:[1,0]
	v_pk_mul_f32 v[244:245], v[244:245], s[8:9] op_sel_hi:[1,0]
	v_pk_add_f32 v[234:235], v[234:235], v[238:239]
	v_pk_add_f32 v[236:237], v[236:237], v[240:241]
	v_pk_fma_f32 v[208:209], v[208:209], v[234:235], v[242:243]
	v_pk_fma_f32 v[210:211], v[210:211], v[236:237], v[244:245]
	v_pk_add_f32 v[246:247], v[246:247], v[208:209]
	v_pk_add_f32 v[246:247], v[246:247], v[210:211]
	v_cvt_pk_f32_fp8_e32 v[234:235], v164
	v_cvt_pk_f32_fp8_sdwa v[236:237], v164 src0_sel:WORD_1
	v_cvt_pk_f32_fp8_e32 v[238:239], v165
	v_cvt_pk_f32_fp8_sdwa v[240:241], v165 src0_sel:WORD_1
	v_lshlrev_b32_e32 v242, 16, v186
	v_and_b32_e32 v243, 0xffff0000, v186
	v_pk_add_f32 v[234:235], v[234:235], v[238:239]
	v_pk_add_f32 v[236:237], v[236:237], v[240:241]
	v_cvt_pk_f32_fp8_e32 v[238:239], v166
	v_cvt_pk_f32_fp8_sdwa v[240:241], v166 src0_sel:WORD_1
	v_lshlrev_b32_e32 v244, 16, v187
	v_and_b32_e32 v245, 0xffff0000, v187
	v_pk_add_f32 v[234:235], v[234:235], v[238:239]
	v_pk_add_f32 v[236:237], v[236:237], v[240:241]
	v_cvt_pk_f32_fp8_e32 v[238:239], v167
	v_cvt_pk_f32_fp8_sdwa v[240:241], v167 src0_sel:WORD_1
	v_pk_mul_f32 v[242:243], v[242:243], s[8:9] op_sel_hi:[1,0]
	v_pk_mul_f32 v[244:245], v[244:245], s[8:9] op_sel_hi:[1,0]
	v_pk_add_f32 v[234:235], v[234:235], v[238:239]
	v_pk_add_f32 v[236:237], v[236:237], v[240:241]
	v_pk_fma_f32 v[212:213], v[212:213], v[234:235], v[242:243]
	v_pk_fma_f32 v[214:215], v[214:215], v[236:237], v[244:245]
	v_pk_add_f32 v[246:247], v[246:247], v[212:213]
	v_pk_add_f32 v[246:247], v[246:247], v[214:215]
	v_cvt_pk_f32_fp8_e32 v[234:235], v168
	v_cvt_pk_f32_fp8_sdwa v[236:237], v168 src0_sel:WORD_1
	v_cvt_pk_f32_fp8_e32 v[238:239], v169
	v_cvt_pk_f32_fp8_sdwa v[240:241], v169 src0_sel:WORD_1
	v_lshlrev_b32_e32 v242, 16, v188
	v_and_b32_e32 v243, 0xffff0000, v188
	v_pk_add_f32 v[234:235], v[234:235], v[238:239]
	v_pk_add_f32 v[236:237], v[236:237], v[240:241]
	v_cvt_pk_f32_fp8_e32 v[238:239], v170
	v_cvt_pk_f32_fp8_sdwa v[240:241], v170 src0_sel:WORD_1
	v_lshlrev_b32_e32 v244, 16, v189
	v_and_b32_e32 v245, 0xffff0000, v189
	v_pk_add_f32 v[234:235], v[234:235], v[238:239]
	v_pk_add_f32 v[236:237], v[236:237], v[240:241]
	v_cvt_pk_f32_fp8_e32 v[238:239], v171
	v_cvt_pk_f32_fp8_sdwa v[240:241], v171 src0_sel:WORD_1
	v_pk_mul_f32 v[242:243], v[242:243], s[8:9] op_sel_hi:[1,0]
	v_pk_mul_f32 v[244:245], v[244:245], s[8:9] op_sel_hi:[1,0]
	v_pk_add_f32 v[234:235], v[234:235], v[238:239]
	v_pk_add_f32 v[236:237], v[236:237], v[240:241]
	v_pk_fma_f32 v[216:217], v[216:217], v[234:235], v[242:243]
	v_pk_fma_f32 v[218:219], v[218:219], v[236:237], v[244:245]
	v_pk_add_f32 v[246:247], v[246:247], v[216:217]
	v_pk_add_f32 v[246:247], v[246:247], v[218:219]
	v_cvt_pk_f32_fp8_e32 v[234:235], v172
	v_cvt_pk_f32_fp8_sdwa v[236:237], v172 src0_sel:WORD_1
	v_cvt_pk_f32_fp8_e32 v[238:239], v173
	v_cvt_pk_f32_fp8_sdwa v[240:241], v173 src0_sel:WORD_1
	v_lshlrev_b32_e32 v242, 16, v190
	v_and_b32_e32 v243, 0xffff0000, v190
	v_pk_add_f32 v[234:235], v[234:235], v[238:239]
	v_pk_add_f32 v[236:237], v[236:237], v[240:241]
	v_cvt_pk_f32_fp8_e32 v[238:239], v174
	v_cvt_pk_f32_fp8_sdwa v[240:241], v174 src0_sel:WORD_1
	v_lshlrev_b32_e32 v244, 16, v191
	v_and_b32_e32 v245, 0xffff0000, v191
	v_pk_add_f32 v[234:235], v[234:235], v[238:239]
	v_pk_add_f32 v[236:237], v[236:237], v[240:241]
	v_cvt_pk_f32_fp8_e32 v[238:239], v175
	v_cvt_pk_f32_fp8_sdwa v[240:241], v175 src0_sel:WORD_1
	v_pk_mul_f32 v[242:243], v[242:243], s[8:9] op_sel_hi:[1,0]
	v_pk_mul_f32 v[244:245], v[244:245], s[8:9] op_sel_hi:[1,0]
	v_pk_add_f32 v[234:235], v[234:235], v[238:239]
	v_pk_add_f32 v[236:237], v[236:237], v[240:241]
	v_pk_fma_f32 v[220:221], v[220:221], v[234:235], v[242:243]
	v_pk_fma_f32 v[222:223], v[222:223], v[236:237], v[244:245]
	v_pk_add_f32 v[246:247], v[246:247], v[220:221]
	v_pk_add_f32 v[246:247], v[246:247], v[222:223]
	v_add_f32_e32 v246, v246, v247
	ds_bpermute_b32 v248, v228, v246
	s_waitcnt lgkmcnt(0)
	v_add_f32_e32 v246, v246, v248
	ds_bpermute_b32 v248, v229, v246
	s_waitcnt lgkmcnt(0)
	v_add_f32_e32 v246, v246, v248
	ds_bpermute_b32 v248, v230, v246
	s_waitcnt lgkmcnt(0)
	v_add_f32_e32 v246, v246, v248
	ds_bpermute_b32 v248, v231, v246
	s_waitcnt lgkmcnt(0)
	v_add_f32_e32 v246, v246, v248
	ds_bpermute_b32 v248, v232, v246
	s_waitcnt lgkmcnt(0)
	v_add_f32_e32 v246, v246, v248
	ds_bpermute_b32 v248, v233, v246
	s_waitcnt lgkmcnt(0)
	v_add_f32_e32 v246, v246, v248
	v_mul_f32_e32 v248, 0xba000000, v246
	v_pk_add_f32 v[192:193], v[192:193], v[248:249] op_sel_hi:[1,0]
	v_pk_add_f32 v[194:195], v[194:195], v[248:249] op_sel_hi:[1,0]
	v_pk_add_f32 v[196:197], v[196:197], v[248:249] op_sel_hi:[1,0]
	v_pk_add_f32 v[198:199], v[198:199], v[248:249] op_sel_hi:[1,0]
	v_pk_add_f32 v[200:201], v[200:201], v[248:249] op_sel_hi:[1,0]
	v_pk_add_f32 v[202:203], v[202:203], v[248:249] op_sel_hi:[1,0]
	v_pk_add_f32 v[204:205], v[204:205], v[248:249] op_sel_hi:[1,0]
	v_pk_add_f32 v[206:207], v[206:207], v[248:249] op_sel_hi:[1,0]
	v_pk_add_f32 v[208:209], v[208:209], v[248:249] op_sel_hi:[1,0]
	v_pk_add_f32 v[210:211], v[210:211], v[248:249] op_sel_hi:[1,0]
	v_pk_add_f32 v[212:213], v[212:213], v[248:249] op_sel_hi:[1,0]
	v_pk_add_f32 v[214:215], v[214:215], v[248:249] op_sel_hi:[1,0]
	v_pk_add_f32 v[216:217], v[216:217], v[248:249] op_sel_hi:[1,0]
	v_pk_add_f32 v[218:219], v[218:219], v[248:249] op_sel_hi:[1,0]
	v_pk_add_f32 v[220:221], v[220:221], v[248:249] op_sel_hi:[1,0]
	v_pk_add_f32 v[222:223], v[222:223], v[248:249] op_sel_hi:[1,0]
	v_pk_mul_f32 v[250:251], v[192:193], v[192:193]
	v_pk_fma_f32 v[250:251], v[194:195], v[194:195], v[250:251]
	v_pk_fma_f32 v[250:251], v[196:197], v[196:197], v[250:251]
	v_pk_fma_f32 v[250:251], v[198:199], v[198:199], v[250:251]
	v_pk_fma_f32 v[250:251], v[200:201], v[200:201], v[250:251]
	v_pk_fma_f32 v[250:251], v[202:203], v[202:203], v[250:251]
	v_pk_fma_f32 v[250:251], v[204:205], v[204:205], v[250:251]
	v_pk_fma_f32 v[250:251], v[206:207], v[206:207], v[250:251]
	v_pk_fma_f32 v[250:251], v[208:209], v[208:209], v[250:251]
	v_pk_fma_f32 v[250:251], v[210:211], v[210:211], v[250:251]
	v_pk_fma_f32 v[250:251], v[212:213], v[212:213], v[250:251]
	v_pk_fma_f32 v[250:251], v[214:215], v[214:215], v[250:251]
	v_pk_fma_f32 v[250:251], v[216:217], v[216:217], v[250:251]
	v_pk_fma_f32 v[250:251], v[218:219], v[218:219], v[250:251]
	v_pk_fma_f32 v[250:251], v[220:221], v[220:221], v[250:251]
	v_pk_fma_f32 v[250:251], v[222:223], v[222:223], v[250:251]
	v_add_f32_e32 v250, v250, v251
	ds_bpermute_b32 v248, v228, v250
	s_waitcnt lgkmcnt(0)
	v_add_f32_e32 v250, v250, v248
	ds_bpermute_b32 v248, v229, v250
	s_waitcnt lgkmcnt(0)
	v_add_f32_e32 v250, v250, v248
	ds_bpermute_b32 v248, v230, v250
	s_waitcnt lgkmcnt(0)
	v_add_f32_e32 v250, v250, v248
	ds_bpermute_b32 v248, v231, v250
	s_waitcnt lgkmcnt(0)
	v_add_f32_e32 v250, v250, v248
	ds_bpermute_b32 v248, v232, v250
	s_waitcnt lgkmcnt(0)
	v_add_f32_e32 v250, v250, v248
	ds_bpermute_b32 v248, v233, v250
	s_waitcnt lgkmcnt(0)
	v_add_f32_e32 v250, v250, v248
	v_mul_f32_e32 v234, 0x3a000000, v250
	v_add_f32_e32 v234, 0x3727c5ac, v234
	v_mul_f32_e32 v235, 0x4f800000, v234
	v_cmp_gt_f32_e32 vcc, s23, v234
	s_nop 1
	v_cndmask_b32_e32 v234, v234, v235, vcc
	v_sqrt_f32_e32 v235, v234
	s_nop 0
	v_add_u32_e32 v236, -1, v235
	v_add_u32_e32 v237, 1, v235
	v_fma_f32 v238, -v236, v235, v234
	v_fma_f32 v239, -v237, v235, v234
	v_cmp_ge_f32_e64 s[0:1], 0, v238
	s_nop 1
	v_cndmask_b32_e64 v235, v235, v236, s[0:1]
	v_cmp_lt_f32_e64 s[0:1], 0, v239
	s_nop 1
	v_cndmask_b32_e64 v235, v235, v237, s[0:1]
	v_mul_f32_e32 v236, 0x37800000, v235
	v_cndmask_b32_e32 v235, v235, v236, vcc
	v_cmp_class_f32_e64 vcc, v234, s22
	s_nop 1
	v_cndmask_b32_e32 v234, v235, v234, vcc
	v_div_scale_f32 v235, s[0:1], v234, v234, 1.0
	v_rcp_f32_e32 v237, v235
	v_div_scale_f32 v236, vcc, 1.0, v234, 1.0
	v_fma_f32 v238, -v235, v237, 1.0
	v_fmac_f32_e32 v237, v238, v237
	v_mul_f32_e32 v238, v236, v237
	v_fma_f32 v239, -v235, v238, v236
	v_fmac_f32_e32 v238, v239, v237
	v_fma_f32 v235, -v235, v238, v236
	v_div_fmas_f32 v235, v235, v237, v238
	v_div_fixup_f32 v234, v235, v234, 1.0
	v_pk_mul_f32 v[192:193], v[192:193], v[234:235] op_sel_hi:[1,0]
	v_pk_mul_f32 v[194:195], v[194:195], v[234:235] op_sel_hi:[1,0]
	v_pk_mul_f32 v[196:197], v[196:197], v[234:235] op_sel_hi:[1,0]
	v_pk_mul_f32 v[198:199], v[198:199], v[234:235] op_sel_hi:[1,0]
	v_pk_mul_f32 v[200:201], v[200:201], v[234:235] op_sel_hi:[1,0]
	v_pk_mul_f32 v[202:203], v[202:203], v[234:235] op_sel_hi:[1,0]
	v_pk_mul_f32 v[204:205], v[204:205], v[234:235] op_sel_hi:[1,0]
	v_pk_mul_f32 v[206:207], v[206:207], v[234:235] op_sel_hi:[1,0]
	v_pk_mul_f32 v[208:209], v[208:209], v[234:235] op_sel_hi:[1,0]
	v_pk_mul_f32 v[210:211], v[210:211], v[234:235] op_sel_hi:[1,0]
	v_pk_mul_f32 v[212:213], v[212:213], v[234:235] op_sel_hi:[1,0]
	v_pk_mul_f32 v[214:215], v[214:215], v[234:235] op_sel_hi:[1,0]
	v_pk_mul_f32 v[216:217], v[216:217], v[234:235] op_sel_hi:[1,0]
	v_pk_mul_f32 v[218:219], v[218:219], v[234:235] op_sel_hi:[1,0]
	v_pk_mul_f32 v[220:221], v[220:221], v[234:235] op_sel_hi:[1,0]
	v_pk_mul_f32 v[222:223], v[222:223], v[234:235] op_sel_hi:[1,0]
	v_pk_fma_f32 v[192:193], v[20:21], v[192:193], v[0:1]
	v_pk_fma_f32 v[194:195], v[22:23], v[194:195], v[2:3]
	v_pk_fma_f32 v[196:197], v[24:25], v[196:197], v[4:5]
	v_pk_fma_f32 v[198:199], v[26:27], v[198:199], v[6:7]
	v_pk_fma_f32 v[200:201], v[32:33], v[200:201], v[8:9]
	v_pk_fma_f32 v[202:203], v[34:35], v[202:203], v[10:11]
	v_pk_fma_f32 v[204:205], v[40:41], v[204:205], v[12:13]
	v_pk_fma_f32 v[206:207], v[42:43], v[206:207], v[14:15]
	v_pk_fma_f32 v[208:209], v[52:53], v[208:209], v[28:29]
	v_pk_fma_f32 v[210:211], v[54:55], v[210:211], v[30:31]
	v_pk_fma_f32 v[212:213], v[56:57], v[212:213], v[36:37]
	v_pk_fma_f32 v[214:215], v[58:59], v[214:215], v[38:39]
	v_pk_fma_f32 v[216:217], v[60:61], v[216:217], v[44:45]
	v_pk_fma_f32 v[218:219], v[62:63], v[218:219], v[46:47]
	v_pk_fma_f32 v[220:221], v[48:49], v[220:221], v[16:17]
	v_pk_fma_f32 v[222:223], v[50:51], v[222:223], v[18:19]
	s_lshl_b32 s0, s2, 13
	s_add_u32 s20, s26, s0
	s_addc_u32 s21, s27, 0
	global_store_dwordx4 v226, v[192:195], s[20:21] nt
	global_store_dwordx4 v226, v[196:199], s[20:21] offset:1024 nt
	global_store_dwordx4 v226, v[200:203], s[20:21] offset:2048 nt
	global_store_dwordx4 v226, v[204:207], s[20:21] offset:3072 nt
	global_store_dwordx4 v227, v[208:211], s[20:21] nt
	global_store_dwordx4 v227, v[212:215], s[20:21] offset:1024 nt
	global_store_dwordx4 v227, v[216:219], s[20:21] offset:2048 nt
	global_store_dwordx4 v227, v[220:223], s[20:21] offset:3072 nt
	s_mov_b32 s2, s3
	s_cmpk_lt_i32 s2, 0x2000
	s_cbranch_scc1 .Lp9_top_A
